# v52 + k_readout: WbT streamed into LDS with global_load_lds_dwordx4 early, mat-vec loop reads LDS instead of 4 serial global-load batches
# baseline (speedup 1.0000x reference)
_Z9k_readoutPKDv4_jPKfPKiPK15HIP_vector_typeIiLj2EES3_S3_S3_PfSA_:
	s_load_dwordx4 s[4:7], s[0:1], 0x0
	s_load_dwordx2 s[8:9], s[0:1], 0x10
	s_load_dwordx2 s[12:13], s[0:1], 0x18
	s_load_dwordx2 s[14:15], s[0:1], 0x28
	v_lshrrev_b32_e32 v53, 6, v0
	v_lshl_or_b32 v44, s2, 2, v53
	v_ashrrev_i32_e32 v45, 31, v44
	v_and_b32_e32 v52, 63, v0
	s_waitcnt lgkmcnt(0)
	v_lshl_add_u64 v[2:3], v[44:45], 2, s[8:9]
	global_load_dword v57, v[2:3], off
	v_mov_b32_e32 v9, 0
	v_lshlrev_b64 v[2:3], 8, v[44:45]
	v_lshl_add_u64 v[2:3], s[6:7], 0, v[2:3]
	v_lshlrev_b32_e32 v46, 2, v52
	v_mov_b32_e32 v47, v9
	v_lshl_add_u64 v[2:3], v[2:3], 0, v[46:47]
	v_add_co_u32_e32 v4, vcc, 0x200000, v2
	s_load_dwordx2 s[6:7], s[0:1], 0x30
	s_nop 0
	v_addc_co_u32_e32 v5, vcc, 0, v3, vcc
	global_load_dword v48, v[2:3], off
	global_load_dword v49, v[4:5], off
	v_lshlrev_b64 v[10:11], 10, v[44:45]
	v_lshl_add_u64 v[10:11], s[12:13], 0, v[10:11]
	v_lshlrev_b32_e32 v12, 3, v52
	v_mov_b32_e32 v13, 0
	v_lshl_add_u64 v[10:11], v[10:11], 0, v[12:13]
	global_load_dwordx2 v[24:25], v[10:11], off
	v_bfe_u32 v54, v0, 5, 1
	s_waitcnt lgkmcnt(0)
	s_load_dword s2, s[6:7], 0x0
	s_movk_i32 s6, 0x80
	v_and_b32_e32 v47, 7, v0
	v_lshlrev_b32_e32 v8, 20, v54
	s_mov_b32 s3, 0
	v_bfe_u32 v55, v0, 3, 2
	v_mbcnt_lo_u32_b32 v56, -1, 0
	s_waitcnt vmcnt(3)
	v_cmp_lt_i32_e32 vcc, s6, v57
	s_and_saveexec_b64 s[6:7], vcc
	s_xor_b64 s[6:7], exec, s[6:7]
	s_cbranch_execz .LBB4_10
	v_lshlrev_b32_e32 v92, 4, v52
	v_mov_b32_e32 v93, 0
	v_lshl_add_u64 v[92:93], s[14:15], 0, v[92:93]
	s_mov_b32 s16, 0x1000
	s_mov_b32 s17, 0
	s_mov_b32 m0, 0x1800
	s_nop 0
	global_load_lds_dwordx4 v[92:93], off
	global_load_lds_dwordx4 v[92:93], off offset:1024
	global_load_lds_dwordx4 v[92:93], off offset:2048
	global_load_lds_dwordx4 v[92:93], off offset:3072
	v_lshl_add_u64 v[92:93], v[92:93], 0, s[16:17]
	s_mov_b32 m0, 0x2800
	s_nop 0
	global_load_lds_dwordx4 v[92:93], off
	global_load_lds_dwordx4 v[92:93], off offset:1024
	global_load_lds_dwordx4 v[92:93], off offset:2048
	global_load_lds_dwordx4 v[92:93], off offset:3072
	v_lshl_add_u64 v[92:93], v[92:93], 0, s[16:17]
	s_mov_b32 m0, 0x3800
	s_nop 0
	global_load_lds_dwordx4 v[92:93], off
	global_load_lds_dwordx4 v[92:93], off offset:1024
	global_load_lds_dwordx4 v[92:93], off offset:2048
	global_load_lds_dwordx4 v[92:93], off offset:3072
	v_lshl_add_u64 v[92:93], v[92:93], 0, s[16:17]
	s_mov_b32 m0, 0x4800
	s_nop 0
	global_load_lds_dwordx4 v[92:93], off
	global_load_lds_dwordx4 v[92:93], off offset:1024
	global_load_lds_dwordx4 v[92:93], off offset:2048
	global_load_lds_dwordx4 v[92:93], off offset:3072
	s_load_dwordx2 s[8:9], s[0:1], 0x20
	v_lshl_add_u64 v[0:1], s[4:5], 0, v[8:9]
	v_lshlrev_b32_e32 v8, 4, v47
	v_lshlrev_b64 v[2:3], 15, v[44:45]
	v_lshl_add_u64 v[16:17], v[0:1], 0, v[8:9]
	v_mbcnt_hi_u32_b32 v1, -1, v56
	s_waitcnt lgkmcnt(0)
	v_lshl_add_u64 v[18:19], s[8:9], 0, v[2:3]
	v_lshlrev_b32_e32 v0, 2, v55
	v_mov_b32_e32 v8, v9
	v_lshlrev_b32_e32 v1, 2, v1
	s_movk_i32 s8, 0x100
	v_mov_b32_e32 v10, v9
	v_mov_b32_e32 v11, v9
	v_mov_b32_e32 v12, v9
	v_mov_b32_e32 v13, v9
	v_mov_b32_e32 v14, v9
	v_mov_b32_e32 v15, v9
	v_and_or_b32 v23, v1, s8, v0
	v_mov_b64_e32 v[0:1], v[8:9]
	v_mov_b32_e32 v22, 0
	v_mov_b64_e32 v[2:3], v[10:11]
	v_mov_b64_e32 v[4:5], v[12:13]
	v_mov_b64_e32 v[6:7], v[14:15]

.LBB4_13:
	s_or_b64 exec, exec, s[8:9]
	v_lshlrev_b32_e32 v58, 9, v53
	v_cmp_lt_i32_e32 vcc, v52, v57
	v_or_b32_e32 v1, 0x800, v58
	v_or_b32_e32 v2, v1, v46
	s_waitcnt vmcnt(0)
	v_lshlrev_b32_e32 v92, 4, v52
	v_mov_b32_e32 v93, 0
	v_lshl_add_u64 v[92:93], s[14:15], 0, v[92:93]
	s_mov_b32 s16, 0x1000
	s_mov_b32 s17, 0
	s_mov_b32 m0, 0x1800
	s_nop 0
	global_load_lds_dwordx4 v[92:93], off
	global_load_lds_dwordx4 v[92:93], off offset:1024
	global_load_lds_dwordx4 v[92:93], off offset:2048
	global_load_lds_dwordx4 v[92:93], off offset:3072
	v_lshl_add_u64 v[92:93], v[92:93], 0, s[16:17]
	s_mov_b32 m0, 0x2800
	s_nop 0
	global_load_lds_dwordx4 v[92:93], off
	global_load_lds_dwordx4 v[92:93], off offset:1024
	global_load_lds_dwordx4 v[92:93], off offset:2048
	global_load_lds_dwordx4 v[92:93], off offset:3072
	v_lshl_add_u64 v[92:93], v[92:93], 0, s[16:17]
	s_mov_b32 m0, 0x3800
	s_nop 0
	global_load_lds_dwordx4 v[92:93], off
	global_load_lds_dwordx4 v[92:93], off offset:1024
	global_load_lds_dwordx4 v[92:93], off offset:2048
	global_load_lds_dwordx4 v[92:93], off offset:3072
	v_lshl_add_u64 v[92:93], v[92:93], 0, s[16:17]
	s_mov_b32 m0, 0x4800
	s_nop 0
	global_load_lds_dwordx4 v[92:93], off
	global_load_lds_dwordx4 v[92:93], off offset:1024
	global_load_lds_dwordx4 v[92:93], off offset:2048
	global_load_lds_dwordx4 v[92:93], off offset:3072
	v_cndmask_b32_e32 v0, v44, v24, vcc
	ds_write2st64_b32 v2, v0, v50 offset1:1
	v_lshlrev_b32_e32 v50, 2, v55
	v_or_b32_e32 v26, v1, v50
	ds_read2_b32 v[0:1], v26 offset1:4
	ds_read2_b32 v[20:21], v26 offset0:16 offset1:20
	v_lshl_or_b32 v45, v47, 4, v8
	v_cndmask_b32_e32 v59, 0, v25, vcc
	ds_read2_b32 v[24:25], v26 offset0:24 offset1:28
	s_waitcnt lgkmcnt(2)
	v_lshl_add_u32 v0, v0, 7, v45
	s_waitcnt lgkmcnt(1)
	v_lshl_add_u32 v16, v20, 7, v45
	global_load_dwordx4 v[8:11], v0, s[4:5]
	v_lshl_add_u32 v20, v21, 7, v45
	global_load_dwordx4 v[16:19], v16, s[4:5]
	v_lshl_add_u32 v0, v1, 7, v45
	global_load_dwordx4 v[12:15], v0, s[4:5]
	v_or_b32_e32 v27, 0x1000, v58
	global_load_dwordx4 v[20:23], v20, s[4:5]
	ds_read2_b32 v[0:1], v26 offset0:8 offset1:12
	s_waitcnt lgkmcnt(1)
	v_lshl_add_u32 v24, v24, 7, v45
	v_or_b32_e32 v30, v27, v46
	v_or_b32_e32 v60, v27, v50
	s_mov_b32 s3, 48
	s_waitcnt lgkmcnt(0)
	v_lshl_add_u32 v0, v0, 7, v45
	global_load_dwordx4 v[4:7], v0, s[4:5]
	v_lshl_add_u32 v0, v1, 7, v45
	global_load_dwordx4 v[0:3], v0, s[4:5]
	ds_read2_b32 v[28:29], v26 offset0:32 offset1:36
	ds_read2_b32 v[26:27], v26 offset0:40 offset1:44
	global_load_dwordx4 v[40:43], v24, s[4:5]
	ds_write2st64_b32 v30, v59, v51 offset1:1
	v_lshl_add_u32 v24, v25, 7, v45
	s_waitcnt lgkmcnt(2)
	v_lshl_add_u32 v25, v28, 7, v45
	v_lshl_add_u32 v28, v29, 7, v45
	s_waitcnt lgkmcnt(1)
	v_lshl_add_u32 v26, v26, 7, v45
	v_lshl_add_u32 v27, v27, 7, v45
	global_load_dwordx4 v[62:65], v24, s[4:5]
	global_load_dwordx4 v[36:39], v25, s[4:5]
	global_load_dwordx4 v[32:35], v28, s[4:5]
	s_nop 0
	global_load_dwordx4 v[28:31], v26, s[4:5]
	s_nop 0
	global_load_dwordx4 v[24:27], v27, s[4:5]
	v_cmp_lt_i32_e32 vcc, 48, v57
	s_waitcnt vmcnt(11)
	v_cvt_f32_f16_e32 v70, v10
	v_cvt_f32_f16_sdwa v71, v10 dst_sel:DWORD dst_unused:UNUSED_PAD src0_sel:WORD_1
	v_cvt_f32_f16_e32 v66, v8
	v_cvt_f32_f16_sdwa v67, v8 dst_sel:DWORD dst_unused:UNUSED_PAD src0_sel:WORD_1
	s_waitcnt vmcnt(9)
	v_cvt_f32_f16_e32 v74, v14
	v_cvt_f32_f16_sdwa v75, v14 dst_sel:DWORD dst_unused:UNUSED_PAD src0_sel:WORD_1
	s_waitcnt vmcnt(8)
	v_cvt_f32_f16_e32 v84, v22
	v_cvt_f32_f16_sdwa v85, v22 dst_sel:DWORD dst_unused:UNUSED_PAD src0_sel:WORD_1
	v_cvt_f32_f16_e32 v91, v23
	v_cvt_f32_f16_e32 v87, v15
	v_cvt_f32_f16_e32 v68, v9
	v_cvt_f32_f16_sdwa v69, v9 dst_sel:DWORD dst_unused:UNUSED_PAD src0_sel:WORD_1
	v_cvt_f32_f16_e32 v72, v12
	v_cvt_f32_f16_sdwa v73, v12 dst_sel:DWORD dst_unused:UNUSED_PAD src0_sel:WORD_1
	v_cvt_f32_f16_e32 v12, v13
	s_waitcnt vmcnt(6)
	v_cvt_f32_f16_e32 v78, v1
	v_cvt_f32_f16_sdwa v79, v1 dst_sel:DWORD dst_unused:UNUSED_PAD src0_sel:WORD_1
	v_cvt_f32_f16_sdwa v1, v23 dst_sel:DWORD dst_unused:UNUSED_PAD src0_sel:WORD_1
	ds_read2_b32 v[22:23], v60 offset1:4
	v_cvt_f32_f16_sdwa v13, v13 dst_sel:DWORD dst_unused:UNUSED_PAD src0_sel:WORD_1
	v_cvt_f32_f16_e32 v61, v11
	v_cvt_f32_f16_sdwa v9, v15 dst_sel:DWORD dst_unused:UNUSED_PAD src0_sel:WORD_1
	v_cvt_f32_f16_sdwa v8, v11 dst_sel:DWORD dst_unused:UNUSED_PAD src0_sel:WORD_1
	s_waitcnt lgkmcnt(0)
	v_mov_b32_e32 v86, v23
	v_pk_fma_f32 v[70:71], v[22:23], v[70:71], 0 op_sel_hi:[0,1,0]
	v_pk_fma_f32 v[70:71], v[86:87], v[74:75], v[70:71] op_sel_hi:[0,1,1]
	ds_read2_b32 v[74:75], v60 offset0:8 offset1:12
	v_cvt_f32_f16_e32 v10, v4
	v_cvt_f32_f16_sdwa v11, v4 dst_sel:DWORD dst_unused:UNUSED_PAD src0_sel:WORD_1
	v_cvt_f32_f16_e32 v14, v5
	v_cvt_f32_f16_sdwa v15, v5 dst_sel:DWORD dst_unused:UNUSED_PAD src0_sel:WORD_1
	v_cvt_f32_f16_e32 v76, v6
	v_cvt_f32_f16_sdwa v77, v6 dst_sel:DWORD dst_unused:UNUSED_PAD src0_sel:WORD_1
	v_cvt_f32_f16_e32 v88, v7
	v_cvt_f32_f16_sdwa v4, v7 dst_sel:DWORD dst_unused:UNUSED_PAD src0_sel:WORD_1
	v_cvt_f32_f16_e32 v6, v0
	v_cvt_f32_f16_sdwa v7, v0 dst_sel:DWORD dst_unused:UNUSED_PAD src0_sel:WORD_1
	v_cvt_f32_f16_e32 v80, v2
	v_cvt_f32_f16_sdwa v81, v2 dst_sel:DWORD dst_unused:UNUSED_PAD src0_sel:WORD_1
	v_pk_fma_f32 v[68:69], v[22:23], v[68:69], 0 op_sel_hi:[0,1,0]
	v_pk_fma_f32 v[66:67], v[22:23], v[66:67], 0 op_sel_hi:[0,1,0]
	v_pk_fma_f32 v[12:13], v[86:87], v[12:13], v[68:69] op_sel_hi:[0,1,1]
	v_pk_fma_f32 v[66:67], v[86:87], v[72:73], v[66:67] op_sel_hi:[0,1,1]
	s_waitcnt lgkmcnt(0)
	v_pk_fma_f32 v[10:11], v[74:75], v[10:11], v[66:67] op_sel_hi:[0,1,1]
	v_pk_fma_f32 v[12:13], v[74:75], v[14:15], v[12:13] op_sel_hi:[0,1,1]
	v_mov_b32_e32 v14, v75
	v_pk_fma_f32 v[66:67], v[74:75], v[76:77], v[70:71] op_sel_hi:[0,1,1]
	v_pk_fma_f32 v[66:67], v[14:15], v[80:81], v[66:67] op_sel_hi:[0,1,1]
	v_pk_fma_f32 v[12:13], v[14:15], v[78:79], v[12:13] op_sel_hi:[0,1,1]
	v_pk_fma_f32 v[6:7], v[14:15], v[6:7], v[10:11] op_sel_hi:[0,1,1]
	s_waitcnt vmcnt(5)
	v_cvt_f32_f16_e32 v10, v40
	v_cvt_f32_f16_sdwa v11, v40 dst_sel:DWORD dst_unused:UNUSED_PAD src0_sel:WORD_1
	v_cvt_f32_f16_e32 v14, v41
	v_cvt_f32_f16_sdwa v15, v41 dst_sel:DWORD dst_unused:UNUSED_PAD src0_sel:WORD_1
	ds_read2_b32 v[40:41], v60 offset0:16 offset1:20
	v_cvt_f32_f16_e32 v89, v3
	v_cvt_f32_f16_sdwa v5, v3 dst_sel:DWORD dst_unused:UNUSED_PAD src0_sel:WORD_1
	v_cvt_f32_f16_e32 v2, v16
	v_cvt_f32_f16_sdwa v3, v16 dst_sel:DWORD dst_unused:UNUSED_PAD src0_sel:WORD_1
	v_cvt_f32_f16_e32 v16, v17
	v_cvt_f32_f16_sdwa v17, v17 dst_sel:DWORD dst_unused:UNUSED_PAD src0_sel:WORD_1
	v_cvt_f32_f16_e32 v90, v19
	v_cvt_f32_f16_e32 v82, v18
	v_cvt_f32_f16_sdwa v83, v18 dst_sel:DWORD dst_unused:UNUSED_PAD src0_sel:WORD_1
	v_cvt_f32_f16_sdwa v0, v19 dst_sel:DWORD dst_unused:UNUSED_PAD src0_sel:WORD_1
	v_cvt_f32_f16_e32 v18, v20
	v_cvt_f32_f16_sdwa v19, v20 dst_sel:DWORD dst_unused:UNUSED_PAD src0_sel:WORD_1
	v_cvt_f32_f16_e32 v20, v21
	v_cvt_f32_f16_sdwa v21, v21 dst_sel:DWORD dst_unused:UNUSED_PAD src0_sel:WORD_1
	s_waitcnt lgkmcnt(0)
	v_pk_fma_f32 v[2:3], v[40:41], v[2:3], v[6:7] op_sel_hi:[0,1,1]
	v_pk_fma_f32 v[6:7], v[40:41], v[16:17], v[12:13] op_sel_hi:[0,1,1]
	v_mov_b32_e32 v16, v41
	v_pk_fma_f32 v[2:3], v[16:17], v[18:19], v[2:3] op_sel_hi:[0,1,1]
	ds_read2_b32 v[18:19], v60 offset0:24 offset1:28
	v_cvt_f32_f16_e32 v68, v42
	v_cvt_f32_f16_sdwa v69, v42 dst_sel:DWORD dst_unused:UNUSED_PAD src0_sel:WORD_1
	v_pk_fma_f32 v[12:13], v[40:41], v[82:83], v[66:67] op_sel_hi:[0,1,1]
	v_pk_fma_f32 v[12:13], v[16:17], v[84:85], v[12:13] op_sel_hi:[0,1,1]
	v_pk_fma_f32 v[6:7], v[16:17], v[20:21], v[6:7] op_sel_hi:[0,1,1]
	s_waitcnt vmcnt(4)
	v_cvt_f32_f16_e32 v20, v62
	v_cvt_f32_f16_sdwa v21, v62 dst_sel:DWORD dst_unused:UNUSED_PAD src0_sel:WORD_1
	v_cvt_f32_f16_e32 v16, v63
	v_cvt_f32_f16_sdwa v17, v63 dst_sel:DWORD dst_unused:UNUSED_PAD src0_sel:WORD_1
	v_cvt_f32_f16_e32 v62, v64
	v_cvt_f32_f16_sdwa v63, v64 dst_sel:DWORD dst_unused:UNUSED_PAD src0_sel:WORD_1
	v_pk_mul_f32 v[8:9], v[22:23], v[8:9]
	s_waitcnt lgkmcnt(0)
	v_pk_fma_f32 v[2:3], v[18:19], v[10:11], v[2:3] op_sel_hi:[0,1,1]
	v_pk_fma_f32 v[10:11], v[18:19], v[68:69], v[12:13] op_sel_hi:[0,1,1]
	v_mov_b32_e32 v12, v19
	s_waitcnt vmcnt(0)
	v_cvt_f32_f16_e32 v66, v26
	v_cvt_f32_f16_sdwa v67, v26 dst_sel:DWORD dst_unused:UNUSED_PAD src0_sel:WORD_1
	v_mul_f32_e32 v22, v22, v61
	v_mul_f32_e32 v26, v23, v87
	v_mov_b32_e32 v23, v8
	v_pk_fma_f32 v[10:11], v[12:13], v[62:63], v[10:11] op_sel_hi:[0,1,1]
	v_cvt_f32_f16_e32 v62, v30
	v_cvt_f32_f16_sdwa v63, v30 dst_sel:DWORD dst_unused:UNUSED_PAD src0_sel:WORD_1
	v_cvt_f32_f16_e32 v72, v31
	v_cvt_f32_f16_sdwa v30, v31 dst_sel:DWORD dst_unused:UNUSED_PAD src0_sel:WORD_1
	v_cvt_f32_f16_sdwa v31, v27 dst_sel:DWORD dst_unused:UNUSED_PAD src0_sel:WORD_1
	v_cvt_f32_f16_e32 v73, v27
	v_mov_b32_e32 v27, v9
	v_pk_add_f32 v[8:9], v[22:23], 0 op_sel_hi:[1,0]
	v_pk_mul_f32 v[4:5], v[74:75], v[4:5]
	v_pk_add_f32 v[8:9], v[8:9], v[26:27]
	v_mul_f32_e32 v22, v74, v88
	v_mov_b32_e32 v23, v4
	v_pk_add_f32 v[8:9], v[8:9], v[22:23]
	v_mul_f32_e32 v4, v75, v89
	v_pk_mul_f32 v[0:1], v[40:41], v[0:1]
	v_pk_add_f32 v[4:5], v[8:9], v[4:5]
	v_mul_f32_e32 v8, v40, v90
	v_mov_b32_e32 v9, v0
	v_pk_add_f32 v[4:5], v[4:5], v[8:9]
	v_mul_f32_e32 v0, v41, v91
	v_pk_fma_f32 v[6:7], v[18:19], v[14:15], v[6:7] op_sel_hi:[0,1,1]
	v_pk_add_f32 v[0:1], v[4:5], v[0:1]
	ds_read2_b32 v[4:5], v60 offset0:32 offset1:36
	v_pk_fma_f32 v[6:7], v[12:13], v[16:17], v[6:7] op_sel_hi:[0,1,1]
	v_pk_fma_f32 v[2:3], v[12:13], v[20:21], v[2:3] op_sel_hi:[0,1,1]
	v_cvt_f32_f16_e32 v12, v36
	v_cvt_f32_f16_sdwa v13, v36 dst_sel:DWORD dst_unused:UNUSED_PAD src0_sel:WORD_1
	v_cvt_f32_f16_e32 v70, v43
	v_cvt_f32_f16_sdwa v42, v43 dst_sel:DWORD dst_unused:UNUSED_PAD src0_sel:WORD_1
	v_cvt_f32_f16_sdwa v43, v65 dst_sel:DWORD dst_unused:UNUSED_PAD src0_sel:WORD_1
	v_cvt_f32_f16_e32 v71, v65
	v_cvt_f32_f16_sdwa v20, v39 dst_sel:DWORD dst_unused:UNUSED_PAD src0_sel:WORD_1
	v_cvt_f32_f16_sdwa v21, v35 dst_sel:DWORD dst_unused:UNUSED_PAD src0_sel:WORD_1
	v_cvt_f32_f16_e32 v14, v37
	v_cvt_f32_f16_sdwa v15, v37 dst_sel:DWORD dst_unused:UNUSED_PAD src0_sel:WORD_1
	v_cvt_f32_f16_e32 v68, v39
	s_waitcnt lgkmcnt(0)
	v_pk_fma_f32 v[2:3], v[4:5], v[12:13], v[2:3] op_sel_hi:[0,1,1]
	ds_read2_b32 v[12:13], v60 offset0:40 offset1:44
	v_cvt_f32_f16_e32 v16, v38
	v_cvt_f32_f16_sdwa v17, v38 dst_sel:DWORD dst_unused:UNUSED_PAD src0_sel:WORD_1
	v_cvt_f32_f16_e32 v69, v35
	v_pk_mul_f32 v[8:9], v[18:19], v[42:43]
	v_cvt_f32_f16_e32 v36, v32
	v_cvt_f32_f16_sdwa v37, v32 dst_sel:DWORD dst_unused:UNUSED_PAD src0_sel:WORD_1
	v_cvt_f32_f16_e32 v32, v33
	v_cvt_f32_f16_sdwa v33, v33 dst_sel:DWORD dst_unused:UNUSED_PAD src0_sel:WORD_1
	v_cvt_f32_f16_e32 v38, v34
	v_cvt_f32_f16_sdwa v39, v34 dst_sel:DWORD dst_unused:UNUSED_PAD src0_sel:WORD_1
	v_mul_f32_e32 v22, v18, v70
	v_mov_b32_e32 v23, v8
	v_cvt_f32_f16_e32 v34, v28
	v_cvt_f32_f16_sdwa v35, v28 dst_sel:DWORD dst_unused:UNUSED_PAD src0_sel:WORD_1
	v_cvt_f32_f16_e32 v28, v29
	v_cvt_f32_f16_sdwa v29, v29 dst_sel:DWORD dst_unused:UNUSED_PAD src0_sel:WORD_1
	v_pk_add_f32 v[0:1], v[0:1], v[22:23]
	v_mul_f32_e32 v8, v19, v71
	v_pk_mul_f32 v[18:19], v[4:5], v[20:21]
	v_cvt_f32_f16_e32 v64, v24
	v_cvt_f32_f16_sdwa v65, v24 dst_sel:DWORD dst_unused:UNUSED_PAD src0_sel:WORD_1
	v_cvt_f32_f16_e32 v24, v25
	v_cvt_f32_f16_sdwa v25, v25 dst_sel:DWORD dst_unused:UNUSED_PAD src0_sel:WORD_1
	v_pk_fma_f32 v[6:7], v[4:5], v[14:15], v[6:7] op_sel_hi:[0,1,1]
	v_mul_f32_e32 v14, v4, v68
	v_pk_add_f32 v[0:1], v[0:1], v[8:9]
	v_mov_b32_e32 v15, v18
	v_pk_fma_f32 v[10:11], v[4:5], v[16:17], v[10:11] op_sel_hi:[0,1,1]
	v_mul_f32_e32 v16, v5, v69
	v_mov_b32_e32 v20, v5
	s_waitcnt lgkmcnt(0)
	v_pk_mul_f32 v[26:27], v[12:13], v[30:31]
	v_pk_add_f32 v[0:1], v[0:1], v[14:15]
	v_mov_b32_e32 v17, v19
	v_mul_f32_e32 v4, v12, v72
	v_pk_fma_f32 v[10:11], v[20:21], v[38:39], v[10:11] op_sel_hi:[0,1,1]
	v_pk_fma_f32 v[6:7], v[20:21], v[32:33], v[6:7] op_sel_hi:[0,1,1]
	v_pk_fma_f32 v[2:3], v[20:21], v[36:37], v[2:3] op_sel_hi:[0,1,1]
	v_pk_add_f32 v[0:1], v[0:1], v[16:17]
	v_mov_b32_e32 v5, v26
	v_mov_b32_e32 v22, v13
	v_mul_f32_e32 v8, v13, v73
	v_pk_add_f32 v[14:15], v[0:1], v[4:5]
	v_pk_fma_f32 v[0:1], v[12:13], v[34:35], v[2:3] op_sel_hi:[0,1,1]
	v_pk_fma_f32 v[2:3], v[12:13], v[28:29], v[6:7] op_sel_hi:[0,1,1]
	v_pk_fma_f32 v[4:5], v[12:13], v[62:63], v[10:11] op_sel_hi:[0,1,1]
	v_mov_b32_e32 v9, v27
	v_pk_fma_f32 v[4:5], v[22:23], v[66:67], v[4:5] op_sel_hi:[0,1,1]
	v_pk_fma_f32 v[2:3], v[22:23], v[24:25], v[2:3] op_sel_hi:[0,1,1]
	v_pk_fma_f32 v[0:1], v[22:23], v[64:65], v[0:1] op_sel_hi:[0,1,1]
	v_pk_add_f32 v[6:7], v[14:15], v[8:9]
	s_and_saveexec_b64 s[8:9], vcc
	s_cbranch_execz .LBB4_17
	s_movk_i32 s10, 0x8c0
	v_or3_b32 v24, v58, v50, s10
	s_mov_b64 s[10:11], 0

.LBB4_20:
	s_or_b64 exec, exec, s[10:11]
	v_mov_b32_e32 v47, 0
	v_lshlrev_b32_e32 v0, 2, v52
	v_add_u32_e32 v0, 0x1800, v0
	s_waitcnt vmcnt(0)
	s_mov_b64 s[0:1], 0
	v_mov_b32_e32 v46, v47
.LBB4_21:
	v_add_u32_e32 v1, s0, v0
	s_waitcnt lgkmcnt(0)
	ds_read_b128 v[26:29], v21
	ds_read_b128 v[30:33], v21 offset:16
	ds_read_b128 v[34:37], v21 offset:32
	ds_read_b128 v[38:41], v21 offset:48
	ds_read_b128 v[54:57], v21 offset:256
	ds_read_b128 v[58:61], v21 offset:272
	ds_read_b128 v[62:65], v21 offset:288
	ds_read_b128 v[66:69], v21 offset:304
	s_waitcnt lgkmcnt(7)
	v_mov_b32_e32 v74, v26
	s_waitcnt lgkmcnt(3)
	v_mov_b32_e32 v75, v54
	v_mov_b32_e32 v54, v27
	v_mov_b32_e32 v26, v28
	v_mov_b32_e32 v27, v56
	v_mov_b32_e32 v56, v29
	v_mov_b32_e32 v28, v30
	s_waitcnt lgkmcnt(2)
	v_mov_b32_e32 v29, v58
	v_mov_b32_e32 v58, v31
	v_mov_b32_e32 v30, v32
	v_mov_b32_e32 v31, v60
	v_mov_b32_e32 v60, v33
	v_mov_b32_e32 v32, v34
	s_waitcnt lgkmcnt(1)
	v_mov_b32_e32 v33, v62
	v_add_u32_e32 v21, 64, v21
	v_mov_b32_e32 v62, v35
	v_mov_b32_e32 v34, v36
	v_mov_b32_e32 v35, v64
	v_mov_b32_e32 v64, v37
	v_mov_b32_e32 v36, v38
	s_waitcnt lgkmcnt(0)
	v_mov_b32_e32 v37, v66
	v_mov_b32_e32 v66, v39
	s_add_u32 s0, s0, 0x1000
	v_mov_b32_e32 v38, v40
	v_mov_b32_e32 v39, v68
	s_addc_u32 s1, s1, 0
	v_mov_b32_e32 v68, v41
	s_cmpk_eq_i32 s0, 0x4000
	ds_read_b32 v2, v1
	ds_read_b32 v4, v1 offset:256
	ds_read_b32 v6, v1 offset:512
	ds_read_b32 v8, v1 offset:768
	ds_read_b32 v10, v1 offset:1024
	ds_read_b32 v12, v1 offset:1280
	ds_read_b32 v14, v1 offset:1536
	ds_read_b32 v16, v1 offset:1792
	ds_read_b32 v18, v1 offset:2048
	ds_read_b32 v20, v1 offset:2304
	ds_read_b32 v22, v1 offset:2560
	ds_read_b32 v24, v1 offset:2816
	ds_read_b32 v42, v1 offset:3072
	ds_read_b32 v50, v1 offset:3328
	ds_read_b32 v70, v1 offset:3584
	ds_read_b32 v72, v1 offset:3840
	s_waitcnt lgkmcnt(15)
	v_pk_fma_f32 v[2:3], v[74:75], v[2:3], v[46:47] op_sel_hi:[1,0,1]
	s_waitcnt lgkmcnt(14)
	v_pk_fma_f32 v[2:3], v[54:55], v[4:5], v[2:3] op_sel_hi:[1,0,1]
	s_waitcnt lgkmcnt(13)
	v_pk_fma_f32 v[2:3], v[26:27], v[6:7], v[2:3] op_sel_hi:[1,0,1]
	s_waitcnt lgkmcnt(12)
	v_pk_fma_f32 v[2:3], v[56:57], v[8:9], v[2:3] op_sel_hi:[1,0,1]
	s_waitcnt lgkmcnt(11)
	v_pk_fma_f32 v[2:3], v[28:29], v[10:11], v[2:3] op_sel_hi:[1,0,1]
	s_waitcnt lgkmcnt(10)
	v_pk_fma_f32 v[2:3], v[58:59], v[12:13], v[2:3] op_sel_hi:[1,0,1]
	s_waitcnt lgkmcnt(9)
	v_pk_fma_f32 v[2:3], v[30:31], v[14:15], v[2:3] op_sel_hi:[1,0,1]
	s_waitcnt lgkmcnt(8)
	v_pk_fma_f32 v[2:3], v[60:61], v[16:17], v[2:3] op_sel_hi:[1,0,1]
	s_waitcnt lgkmcnt(7)
	v_pk_fma_f32 v[2:3], v[32:33], v[18:19], v[2:3] op_sel_hi:[1,0,1]
	s_waitcnt lgkmcnt(6)
	v_pk_fma_f32 v[2:3], v[62:63], v[20:21], v[2:3] op_sel_hi:[1,0,1]
	s_waitcnt lgkmcnt(5)
	v_pk_fma_f32 v[2:3], v[34:35], v[22:23], v[2:3] op_sel_hi:[1,0,1]
	s_waitcnt lgkmcnt(4)
	v_pk_fma_f32 v[2:3], v[64:65], v[24:25], v[2:3] op_sel_hi:[1,0,1]
	s_waitcnt lgkmcnt(3)
	v_pk_fma_f32 v[2:3], v[36:37], v[42:43], v[2:3] op_sel_hi:[1,0,1]
	s_waitcnt lgkmcnt(2)
	v_pk_fma_f32 v[2:3], v[66:67], v[50:51], v[2:3] op_sel_hi:[1,0,1]
	s_waitcnt lgkmcnt(1)
	v_pk_fma_f32 v[2:3], v[38:39], v[70:71], v[2:3] op_sel_hi:[1,0,1]
	s_waitcnt lgkmcnt(0)
	v_pk_fma_f32 v[46:47], v[68:69], v[72:73], v[2:3] op_sel_hi:[1,0,1]
	s_cbranch_scc0 .LBB4_21
	v_mov_b32_e32 v0, v49
	v_mov_b32_e32 v1, v48
	v_pk_mul_f32 v[2:3], v[48:49], v[46:47] op_sel_hi:[1,0]
	v_pk_mul_f32 v[4:5], v[0:1], v[46:47] op_sel:[0,1]
	ds_bpermute_b32 v2, v19, v2
	ds_bpermute_b32 v3, v19, v3
	ds_bpermute_b32 v4, v19, v4
	ds_bpermute_b32 v5, v19, v5
	v_cmp_eq_u32_e32 vcc, 0, v52
	s_waitcnt lgkmcnt(2)
	v_pk_fma_f32 v[2:3], v[48:49], v[46:47], v[2:3] op_sel_hi:[1,0,1]
	ds_bpermute_b32 v6, v15, v2
	s_waitcnt lgkmcnt(1)
	v_pk_fma_f32 v[0:1], v[0:1], v[46:47], v[4:5] op_sel:[0,1,0]
	ds_bpermute_b32 v7, v15, v3
	ds_bpermute_b32 v4, v15, v0
	ds_bpermute_b32 v5, v15, v1
	s_waitcnt lgkmcnt(2)
	v_pk_add_f32 v[2:3], v[2:3], v[6:7]
	ds_bpermute_b32 v6, v13, v2
	s_waitcnt lgkmcnt(1)
	v_pk_add_f32 v[0:1], v[0:1], v[4:5]
	ds_bpermute_b32 v7, v13, v3
	ds_bpermute_b32 v4, v13, v0
	ds_bpermute_b32 v5, v13, v1
	s_waitcnt lgkmcnt(2)
	v_pk_add_f32 v[2:3], v[2:3], v[6:7]
	ds_bpermute_b32 v6, v11, v2
	s_waitcnt lgkmcnt(1)
	v_pk_add_f32 v[0:1], v[0:1], v[4:5]
	ds_bpermute_b32 v7, v11, v3
	ds_bpermute_b32 v4, v11, v0
	ds_bpermute_b32 v5, v11, v1
	s_waitcnt lgkmcnt(2)
	v_pk_add_f32 v[2:3], v[2:3], v[6:7]
	ds_bpermute_b32 v6, v9, v2
	s_waitcnt lgkmcnt(1)
	v_pk_add_f32 v[0:1], v[0:1], v[4:5]
	ds_bpermute_b32 v7, v9, v3
	ds_bpermute_b32 v4, v9, v0
	ds_bpermute_b32 v5, v9, v1
	s_waitcnt lgkmcnt(2)
	v_pk_add_f32 v[2:3], v[2:3], v[6:7]
	ds_bpermute_b32 v6, v17, v2
	s_waitcnt lgkmcnt(1)
	v_pk_add_f32 v[0:1], v[0:1], v[4:5]
	ds_bpermute_b32 v7, v17, v3
	ds_bpermute_b32 v4, v17, v0
	ds_bpermute_b32 v5, v17, v1
	s_and_saveexec_b64 s[0:1], vcc
	s_cbranch_execz .LBB4_24
	v_lshlrev_b32_e32 v8, 1, v44
	v_ashrrev_i32_e32 v9, 31, v8
	v_lshlrev_b64 v[8:9], 2, v[8:9]
	s_waitcnt lgkmcnt(2)
	v_pk_add_f32 v[2:3], v[2:3], v[6:7]
	v_lshl_add_u64 v[10:11], s[4:5], 0, v[8:9]
	v_pk_add_f32 v[2:3], s[2:3], v[2:3] op_sel_hi:[0,1]
	s_waitcnt lgkmcnt(0)
	v_pk_add_f32 v[0:1], v[0:1], v[4:5]
	global_store_dwordx2 v[10:11], v[2:3], off
	v_lshl_add_u64 v[2:3], s[6:7], 0, v[8:9]
	v_pk_add_f32 v[0:1], s[2:3], v[0:1] op_sel_hi:[0,1]
	global_store_dwordx2 v[2:3], v[0:1], off

	.amdhsa_kernel _Z9k_readoutPKDv4_jPKfPKiPK15HIP_vector_typeIiLj2EES3_S3_S3_PfSA_
		.amdhsa_group_segment_fixed_size 22528
		.amdhsa_private_segment_fixed_size 0
		.amdhsa_kernarg_size 72
		.amdhsa_user_sgpr_count 2
		.amdhsa_user_sgpr_dispatch_ptr 0
		.amdhsa_user_sgpr_queue_ptr 0
		.amdhsa_user_sgpr_kernarg_segment_ptr 1
		.amdhsa_user_sgpr_dispatch_id 0
		.amdhsa_user_sgpr_kernarg_preload_length 0
		.amdhsa_user_sgpr_kernarg_preload_offset 0
		.amdhsa_user_sgpr_private_segment_size 0
		.amdhsa_uses_dynamic_stack 0
		.amdhsa_enable_private_segment 0
		.amdhsa_system_sgpr_workgroup_id_x 1
		.amdhsa_system_sgpr_workgroup_id_y 0
		.amdhsa_system_sgpr_workgroup_id_z 0
		.amdhsa_system_sgpr_workgroup_info 0
		.amdhsa_system_vgpr_workitem_id 0
		.amdhsa_next_free_vgpr 94
		.amdhsa_next_free_sgpr 18
		.amdhsa_accum_offset 96
		.amdhsa_reserve_vcc 1
		.amdhsa_float_round_mode_32 0
		.amdhsa_float_round_mode_16_64 0
		.amdhsa_float_denorm_mode_32 3
		.amdhsa_float_denorm_mode_16_64 3
		.amdhsa_dx10_clamp 1
		.amdhsa_ieee_mode 1
		.amdhsa_fp16_overflow 0
		.amdhsa_tg_split 0
		.amdhsa_exception_fp_ieee_invalid_op 0
		.amdhsa_exception_fp_denorm_src 0
		.amdhsa_exception_fp_ieee_div_zero 0
		.amdhsa_exception_fp_ieee_overflow 0
		.amdhsa_exception_fp_ieee_underflow 0
		.amdhsa_exception_fp_ieee_inexact 0
		.amdhsa_exception_int_div_zero 0
	.end_amdhsa_kernel

amdhsa.kernels:
  - .agpr_count:     0
    .args:
      - .actual_access:  read_only
        .address_space:  global
        .offset:         0
        .size:           8
        .value_kind:     global_buffer
      - .actual_access:  read_only
        .address_space:  global
        .offset:         8
        .size:           8
        .value_kind:     global_buffer
      - .actual_access:  read_only
        .address_space:  global
        .offset:         16
        .size:           8
        .value_kind:     global_buffer
      - .actual_access:  write_only
        .address_space:  global
        .offset:         24
        .size:           8
        .value_kind:     global_buffer
      - .actual_access:  write_only
        .address_space:  global
        .offset:         32
        .size:           8
        .value_kind:     global_buffer
      - .actual_access:  write_only
        .address_space:  global
        .offset:         40
        .size:           8
        .value_kind:     global_buffer
      - .actual_access:  read_only
        .address_space:  global
        .offset:         48
        .size:           8
        .value_kind:     global_buffer
      - .actual_access:  read_only
        .address_space:  global
        .offset:         56
        .size:           8
        .value_kind:     global_buffer
      - .actual_access:  read_only
        .address_space:  global
        .offset:         64
        .size:           8
        .value_kind:     global_buffer
      - .actual_access:  write_only
        .address_space:  global
        .offset:         72
        .size:           8
        .value_kind:     global_buffer
    .group_segment_fixed_size: 0
    .kernarg_segment_align: 8
    .kernarg_segment_size: 80
    .language:       OpenCL C
    .language_version:
      - 2
      - 0
    .max_flat_workgroup_size: 256
    .name:           _Z8k_phase1PKfS0_S0_PDv4_jS2_PiS3_P15HIP_vector_typeIiLj2EES0_Pf
    .private_segment_fixed_size: 0
    .sgpr_count:     18
    .sgpr_spill_count: 0
    .symbol:         _Z8k_phase1PKfS0_S0_PDv4_jS2_PiS3_P15HIP_vector_typeIiLj2EES0_Pf.kd
    .uniform_work_group_size: 1
    .uses_dynamic_stack: false
    .vgpr_count:     19
    .vgpr_spill_count: 0
    .wavefront_size: 64
  - .agpr_count:     0
    .args:
      - .actual_access:  read_only
        .address_space:  global
        .offset:         0
        .size:           8
        .value_kind:     global_buffer
      - .actual_access:  read_only
        .address_space:  global
        .offset:         8
        .size:           8
        .value_kind:     global_buffer
      - .actual_access:  read_only
        .address_space:  global
        .offset:         16
        .size:           8
        .value_kind:     global_buffer
      - .actual_access:  read_only
        .address_space:  global
        .offset:         24
        .size:           8
        .value_kind:     global_buffer
      - .address_space:  global
        .offset:         32
        .size:           8
        .value_kind:     global_buffer
      - .actual_access:  write_only
        .address_space:  global
        .offset:         40
        .size:           8
        .value_kind:     global_buffer
      - .actual_access:  write_only
        .address_space:  global
        .offset:         48
        .size:           8
        .value_kind:     global_buffer
      - .actual_access:  write_only
        .address_space:  global
        .offset:         56
        .size:           8
        .value_kind:     global_buffer
      - .actual_access:  read_only
        .address_space:  global
        .offset:         64
        .size:           8
        .value_kind:     global_buffer
      - .actual_access:  write_only
        .address_space:  global
        .offset:         72
        .size:           8
        .value_kind:     global_buffer
      - .actual_access:  write_only
        .address_space:  global
        .offset:         80
        .size:           8
        .value_kind:     global_buffer
    .group_segment_fixed_size: 90112
    .kernarg_segment_align: 8
    .kernarg_segment_size: 88
    .language:       OpenCL C
    .language_version:
      - 2
      - 0
    .max_flat_workgroup_size: 768
    .name:           _Z7k_gemm1PKfS0_PKDv4_jPKiPiS6_P15HIP_vector_typeIiLj2EEPDF16_S0_S6_S9_
    .private_segment_fixed_size: 0
    .sgpr_count:     48
    .sgpr_spill_count: 0
    .symbol:         _Z7k_gemm1PKfS0_PKDv4_jPKiPiS6_P15HIP_vector_typeIiLj2EEPDF16_S0_S6_S9_.kd
    .uniform_work_group_size: 1
    .uses_dynamic_stack: false
    .vgpr_count:     168
    .vgpr_spill_count: 0
    .wavefront_size: 64
  - .agpr_count:     0
    .args:
      - .actual_access:  read_only
        .address_space:  global
        .offset:         0
        .size:           8
        .value_kind:     global_buffer
      - .actual_access:  read_only
        .address_space:  global
        .offset:         8
        .size:           8
        .value_kind:     global_buffer
      - .actual_access:  read_only
        .address_space:  global
        .offset:         16
        .size:           8
        .value_kind:     global_buffer
      - .actual_access:  read_only
        .address_space:  global
        .offset:         24
        .size:           8
        .value_kind:     global_buffer
      - .actual_access:  read_only
        .address_space:  global
        .offset:         32
        .size:           8
        .value_kind:     global_buffer
      - .actual_access:  read_only
        .address_space:  global
        .offset:         40
        .size:           8
        .value_kind:     global_buffer
      - .actual_access:  write_only
        .address_space:  global
        .offset:         48
        .size:           8
        .value_kind:     global_buffer
    .group_segment_fixed_size: 12576
    .kernarg_segment_align: 8
    .kernarg_segment_size: 56
    .language:       OpenCL C
    .language_version:
      - 2
      - 0
    .max_flat_workgroup_size: 256
    .name:           _Z8k_agg1g2PKDv4_jPKiS3_PK15HIP_vector_typeIiLj2EEPKfS1_PDF16_
    .private_segment_fixed_size: 0
    .sgpr_count:     52
    .sgpr_spill_count: 0
    .symbol:         _Z8k_agg1g2PKDv4_jPKiS3_PK15HIP_vector_typeIiLj2EEPKfS1_PDF16_.kd
    .uniform_work_group_size: 1
    .uses_dynamic_stack: false
    .vgpr_count:     126
    .vgpr_spill_count: 0
    .wavefront_size: 64
  - .agpr_count:     0
    .args:
      - .actual_access:  read_only
        .address_space:  global
        .offset:         0
        .size:           8
        .value_kind:     global_buffer
      - .actual_access:  read_only
        .address_space:  global
        .offset:         8
        .size:           8
        .value_kind:     global_buffer
      - .actual_access:  read_only
        .address_space:  global
        .offset:         16
        .size:           8
        .value_kind:     global_buffer
      - .actual_access:  read_only
        .address_space:  global
        .offset:         24
        .size:           8
        .value_kind:     global_buffer
      - .actual_access:  read_only
        .address_space:  global
        .offset:         32
        .size:           8
        .value_kind:     global_buffer
      - .actual_access:  write_only
        .address_space:  global
        .offset:         40
        .size:           8
        .value_kind:     global_buffer
      - .actual_access:  write_only
        .address_space:  global
        .offset:         48
        .size:           8
        .value_kind:     global_buffer
      - .actual_access:  write_only
        .address_space:  global
        .offset:         56
        .size:           8
        .value_kind:     global_buffer
    .group_segment_fixed_size: 0
    .kernarg_segment_align: 8
    .kernarg_segment_size: 64
    .language:       OpenCL C
    .language_version:
      - 2
      - 0
    .max_flat_workgroup_size: 256
    .name:           _Z6k_agg2PKDv4_jPKiS3_PK15HIP_vector_typeIiLj2EEPKfPfSA_PS_
    .private_segment_fixed_size: 0
    .sgpr_count:     18
    .sgpr_spill_count: 0
    .symbol:         _Z6k_agg2PKDv4_jPKiS3_PK15HIP_vector_typeIiLj2EEPKfPfSA_PS_.kd
    .uniform_work_group_size: 1
    .uses_dynamic_stack: false
    .vgpr_count:     62
    .vgpr_spill_count: 0
    .wavefront_size: 64
  - .agpr_count:     0
    .args:
      - .actual_access:  read_only
        .address_space:  global
        .offset:         0
        .size:           8
        .value_kind:     global_buffer
      - .actual_access:  read_only
        .address_space:  global
        .offset:         8
        .size:           8
        .value_kind:     global_buffer
      - .actual_access:  read_only
        .address_space:  global
        .offset:         16
        .size:           8
        .value_kind:     global_buffer
      - .actual_access:  read_only
        .address_space:  global
        .offset:         24
        .size:           8
        .value_kind:     global_buffer
      - .actual_access:  read_only
        .address_space:  global
        .offset:         32
        .size:           8
        .value_kind:     global_buffer
      - .actual_access:  read_only
        .address_space:  global
        .offset:         40
        .size:           8
        .value_kind:     global_buffer
      - .actual_access:  read_only
        .address_space:  global
        .offset:         48
        .size:           8
        .value_kind:     global_buffer
      - .actual_access:  write_only
        .address_space:  global
        .offset:         56
        .size:           8
        .value_kind:     global_buffer
      - .actual_access:  write_only
        .address_space:  global
        .offset:         64
        .size:           8
        .value_kind:     global_buffer
    .group_segment_fixed_size: 22528
    .kernarg_segment_align: 8
    .kernarg_segment_size: 72
    .language:       OpenCL C
    .language_version:
      - 2
      - 0
    .max_flat_workgroup_size: 256
    .name:           _Z9k_readoutPKDv4_jPKfPKiPK15HIP_vector_typeIiLj2EES3_S3_S3_PfSA_
    .private_segment_fixed_size: 0
    .sgpr_count:     24
    .sgpr_spill_count: 0
    .symbol:         _Z9k_readoutPKDv4_jPKfPKiPK15HIP_vector_typeIiLj2EES3_S3_S3_PfSA_.kd
    .uniform_work_group_size: 1
    .uses_dynamic_stack: false
    .vgpr_count:     94
    .vgpr_spill_count: 0
    .wavefront_size: 64
